# q/k-bound units moved off the 16 forget-scan workgroups; GU-tail weight conversion taken by workgroups without a fifth GEMM unit
# speedup vs baseline: 1.0034x; 1.0034x over previous
; __global__ void __launch_bounds__(NWAVES * 64, 2) mega_fwd(Args args) {
;     ...
;             for (int bh = F.bx; bh < 16; bh += F.G) fscan_unit(F, F.l, bh);
;             for (int u = F.bx; u < 256; u += F.G) qknorm_unit(F, u, F.ctl + CW_QKN + F.l * 32);
.LBB0_942:
	s_andn2_b64 vcc, exec, s[12:13]
	s_cbranch_vccnz .LBB0_954
	s_sub_i32 s26, s26, 16
	s_cmpk_gt_u32 s26, 0xff
	s_cbranch_scc1 .LBB0_954
	s_lshl_b32 s0, s28, 5
	s_ashr_i32 s1, s0, 31
	s_lshl_b64 s[0:1], s[0:1], 2
	s_add_u32 s0, s10, s0
	s_addc_u32 s1, s11, s1
	s_add_u32 s6, s0, 0x8000
	s_addc_u32 s7, s1, 0
	s_branch .LBB0_945
.LBB0_944:
	s_or_b64 exec, exec, s[0:1]
	s_addk_i32 s26, 0xf0
	s_cmpk_lt_i32 s26, 0x100
	s_cbranch_scc0 .LBB0_954

; #define LAS __attribute__((address_space(3)))
;     LAS unsigned* scr = (LAS unsigned*)(F.lds + F.wave * 16384);
;     if (gw < 0) { gw = F.vcu * NWAVES + F.wave; NGW = F.G * NWAVES; }
;     const int gi = F.lane & 15;
;     int it = n0 + gw; if (it >= n1) return;
;     CvItem da = cv_decode(F, l, it, gi), db = da; f32x4 va[16], vb[16]; cv_load(da, F.lane, va);
; __global__ void __launch_bounds__(NWAVES * 64, 2) mega_fwd(Args args) {
;     ...
;             if (F.l + 1 < NLAYER) { p_convert(F, F.l + 1, CV_WIN, CV_DENSE);
.LBB0_3538:
	s_cmp_lt_i32 s34, 3
	s_cbranch_scc0 .LBB0_3803
	s_ashr_i32 s23, s31, 6
	s_sub_i32 s10, 0xff, s57
	s_lshl_b32 s10, s10, 3
	s_add_i32 s10, s10, s23
	s_cmpk_gt_i32 s10, 0x10f
	s_cbranch_scc1 .LBB0_3803
	s_add_i32 s12, s34, 1
	s_add_i32 s58, s10, 0x350
	v_and_b32_e32 v1, 15, v132
	s_cmpk_gt_i32 s10, 0xffef
	s_mul_hi_i32 s36, s12, 0xd10000
	s_mul_i32 s37, s12, 0xd10000
	s_cbranch_scc0 .LBB0_3550
	s_cmp_lt_u32 s10, 0xfffffcb0
	s_cbranch_scc0 .LBB0_3551
	s_cmpk_gt_u32 s58, 0x44f
	s_cbranch_scc0 .LBB0_3553
	v_cmp_ne_u32_e32 vcc, 0, v1
	s_and_saveexec_b64 s[0:1], vcc
	s_xor_b64 s[0:1], exec, s[0:1]
	s_cbranch_execz .LBB0_3547
	v_cmp_gt_u32_e32 vcc, 9, v1
	v_mov_b64_e32 v[66:67], 0
	s_and_saveexec_b64 s[2:3], vcc
	s_cbranch_execz .LBB0_3546
	s_add_i32 s4, s30, 0x208a8
	v_mov_b32_e32 v0, s4
	ds_read2_b32 v[4:5], v0 offset1:1
	s_ashr_i32 s13, s12, 31
	s_lshl_b64 s[4:5], s[12:13], 17
	v_lshlrev_b32_e32 v2, 4, v1
	s_waitcnt lgkmcnt(0)
	v_readfirstlane_b32 s11, v4
	v_readfirstlane_b32 s13, v5
	s_add_u32 s4, s11, s4
	s_addc_u32 s5, s13, s5
	v_lshl_add_u64 v[4:5], s[4:5], 0, v[2:3]
	v_lshl_add_u64 v[66:67], v[4:5], 0, -16
